# proj phase with 24 helpers / 232 workers (13 rounds), helpers convert 10752 layer-0 items; prologue takes the remaining 7424
# baseline (speedup 1.0000x reference)
;     ...
;         int it = gw; TrDesc dA, dB; f32x4 vA[16], vB[16];
;         if (it < NIT) { dA = decode(NIT - 1 - it); tr_load(dA, vA); }
;         while (it < NIT) {
;             const int itB = it + NGW;
;             if (itB < NIT) { dB = decode(NIT - 1 - itB); tr_load(dB, vB); }
;             tr_finish(dA, vA, scr, lane);
;             if (itB >= NIT) break;
;             const int itA = itB + NGW;
;             if (itA < NIT) { dA = decode(NIT - 1 - itA); tr_load(dA, vA); }
;             tr_finish(dB, vB, scr, lane);
;             it = itA;
;         }
.LBB0_72:
	s_cmp_gt_i32 s42, 0xfcff
	s_cbranch_scc1 .LBB0_70
	s_add_i32 s44, s42, s48
	s_cmp_lt_i32 s44, 0x800
	s_cbranch_scc1 .Lpt_1
	s_cmp_ge_i32 s44, 0xc880
	s_cbranch_scc1 .Lpt_1
	s_add_i32 s44, s44, 0xc080

; #define LAS __attribute__((address_space(3)))
; #define LDS_WAIT() asm volatile("s_waitcnt lgkmcnt(0)" ::: "memory")
; __device__ __forceinline__ unsigned pk_fp8x4(float a, float b, float c, float d) { int p = __builtin_amdgcn_cvt_pk_fp8_f32(sat8(a), sat8(b), 0, false); p = __builtin_amdgcn_cvt_pk_fp8_f32(sat8(c), sat8(d), p, true); return (unsigned)p; }
; __device__ __forceinline__ void tr_finish(const TrDesc& d, f32x4 (&v)[16], LAS float* scr, int lane) {
;     ...
;     const int d0 = d.rope ? 8 * (q4 & 7) + (q4 >> 3) : 4 * q4, ds = d.rope ? 2 : 1;
;     { LAS float* rp = scr + kk * 65 + d0;
; #pragma unroll
;         for (int i = 0; i < 16; ++i) { rp[4 * i * 65] = v[i][0]; rp[4 * i * 65 + ds] = v[i][1]; rp[4 * i * 65 + 2 * ds] = v[i][2]; rp[4 * i * 65 + 3 * ds] = v[i][3]; } }
;     LDS_WAIT(); asm volatile("" ::: "memory");
;     if (d.f8) {
;         const int c = lane & 3, nl = lane >> 2; const LAS float* sp = scr + (16 * c) * 65 + nl; unsigned char* dp = d.dst + (size_t)nl * d.K + 16 * c;
; #pragma unroll
;         for (int j = 0; j < 4; ++j) { u32x4 o;
;             o.x = pk_fp8x4(sp[0 * 65 + 16 * j] * 32.0f, sp[1 * 65 + 16 * j] * 32.0f, sp[2 * 65 + 16 * j] * 32.0f, sp[3 * 65 + 16 * j] * 32.0f);
;             o.y = pk_fp8x4(sp[4 * 65 + 16 * j] * 32.0f, sp[5 * 65 + 16 * j] * 32.0f, sp[6 * 65 + 16 * j] * 32.0f, sp[7 * 65 + 16 * j] * 32.0f);
;             o.z = pk_fp8x4(sp[8 * 65 + 16 * j] * 32.0f, sp[9 * 65 + 16 * j] * 32.0f, sp[10 * 65 + 16 * j] * 32.0f, sp[11 * 65 + 16 * j] * 32.0f);
;             o.w = pk_fp8x4(sp[12 * 65 + 16 * j] * 32.0f, sp[13 * 65 + 16 * j] * 32.0f, sp[14 * 65 + 16 * j] * 32.0f, sp[15 * 65 + 16 * j] * 32.0f);
.LBB0_108:
	s_or_b64 exec, exec, s[22:23]
	s_cmp_eq_u32 s43, 0
	s_cselect_b64 vcc, -1, 0
	s_cmp_lg_u32 s43, 0
	s_cselect_b64 s[22:23], -1, 0
	v_cndmask_b32_e64 v2, 0, 1, s[22:23]
	s_and_b64 s[22:23], s[22:23], exec
	v_cndmask_b32_e32 v0, v140, v136, vcc
	s_cselect_b32 s0, 2, 1
	v_lshl_add_u32 v0, v0, 2, v141
	s_lshl_b32 s3, s0, 2
	v_add_u32_e32 v3, s3, v0
	v_lshlrev_b32_e64 v2, v2, 3
	s_waitcnt vmcnt(15)
	ds_write_b32 v3, v5
	v_lshl_add_u32 v3, s0, 3, v0
	v_lshl_add_u32 v2, v2, 2, v0
	v_subrev_u32_e32 v146, s3, v3
	ds_write_b32 v0, v4
	ds_write_b32 v3, v6
	ds_write_b32 v2, v7
	s_waitcnt vmcnt(14)
	ds_write_b32 v0, v8 offset:1040
	ds_write_b32 v146, v9 offset:1040
	ds_write_b32 v3, v10 offset:1040
	ds_write_b32 v2, v11 offset:1040
	s_waitcnt vmcnt(13)
	ds_write_b32 v0, v12 offset:2080
	ds_write_b32 v146, v13 offset:2080
	ds_write_b32 v3, v14 offset:2080
	ds_write_b32 v2, v15 offset:2080
	s_waitcnt vmcnt(12)
	ds_write_b32 v0, v16 offset:3120
	ds_write_b32 v146, v17 offset:3120
	ds_write_b32 v3, v18 offset:3120
	ds_write_b32 v2, v19 offset:3120
	s_waitcnt vmcnt(11)
	ds_write_b32 v0, v20 offset:4160
	ds_write_b32 v146, v21 offset:4160
	ds_write_b32 v3, v22 offset:4160
	ds_write_b32 v2, v23 offset:4160
	s_waitcnt vmcnt(10)
	ds_write_b32 v0, v24 offset:5200
	ds_write_b32 v146, v25 offset:5200
	ds_write_b32 v3, v26 offset:5200
	ds_write_b32 v2, v27 offset:5200
	s_waitcnt vmcnt(9)
	ds_write_b32 v0, v28 offset:6240
	ds_write_b32 v146, v29 offset:6240
	ds_write_b32 v3, v30 offset:6240
	ds_write_b32 v2, v31 offset:6240
	s_waitcnt vmcnt(8)
	ds_write_b32 v0, v32 offset:7280
	ds_write_b32 v146, v33 offset:7280
	ds_write_b32 v3, v34 offset:7280
	ds_write_b32 v2, v35 offset:7280
	s_waitcnt vmcnt(7)
	ds_write_b32 v0, v36 offset:8320
	ds_write_b32 v146, v37 offset:8320
	ds_write_b32 v3, v38 offset:8320
	ds_write_b32 v2, v39 offset:8320
	s_waitcnt vmcnt(6)
	ds_write_b32 v0, v40 offset:9360
	ds_write_b32 v146, v41 offset:9360
	ds_write_b32 v3, v42 offset:9360
	ds_write_b32 v2, v43 offset:9360
	s_waitcnt vmcnt(5)
	ds_write_b32 v0, v44 offset:10400
	ds_write_b32 v146, v45 offset:10400
	ds_write_b32 v3, v46 offset:10400
	ds_write_b32 v2, v47 offset:10400
	s_waitcnt vmcnt(4)
	ds_write_b32 v0, v48 offset:11440
	ds_write_b32 v146, v49 offset:11440
	ds_write_b32 v3, v50 offset:11440
	ds_write_b32 v2, v51 offset:11440
	s_waitcnt vmcnt(3)
	ds_write_b32 v0, v52 offset:12480
	ds_write_b32 v146, v53 offset:12480
	ds_write_b32 v3, v54 offset:12480
	ds_write_b32 v2, v55 offset:12480
	s_waitcnt vmcnt(2)
	ds_write_b32 v0, v56 offset:13520
	ds_write_b32 v146, v57 offset:13520
	ds_write_b32 v3, v58 offset:13520
	ds_write_b32 v2, v59 offset:13520
	s_waitcnt vmcnt(1)
	ds_write_b32 v0, v60 offset:14560
	ds_write_b32 v146, v61 offset:14560
	ds_write_b32 v3, v62 offset:14560
	ds_write_b32 v2, v63 offset:14560
	s_waitcnt vmcnt(0)
	ds_write_b32 v0, v64 offset:15600
	ds_write_b32 v146, v65 offset:15600
	ds_write_b32 v3, v66 offset:15600
	ds_write_b32 v2, v67 offset:15600
	s_waitcnt lgkmcnt(0)
	ds_read2_b32 v[2:3], v142 offset1:16
	ds_read2_b32 v[148:149], v142 offset0:65 offset1:81
	ds_read2_b32 v[154:155], v142 offset0:130 offset1:146
	ds_read2_b32 v[156:157], v142 offset0:195 offset1:211
	v_mov_b32_e32 v150, 0
	s_waitcnt lgkmcnt(3)
	v_mul_f32_e32 v0, 0x42000000, v2
	s_waitcnt lgkmcnt(2)
	v_mul_f32_e32 v2, 0x42000000, v148
	v_med3_f32 v0, v0, s41, v143
	s_waitcnt lgkmcnt(0)
	v_mul_f32_e32 v147, 0x42000000, v156
	v_med3_f32 v2, v2, s41, v143
	v_cvt_pk_fp8_f32 v150, v0, v2
	v_med3_f32 v2, v147, s41, v143
	v_add_u32_e32 v147, 0x400, v142
	ds_read2_b32 v[160:161], v147 offset0:4 offset1:20
	ds_read2_b32 v[162:163], v147 offset0:69 offset1:85
	ds_read2_b32 v[164:165], v147 offset0:134 offset1:150
	ds_read2_b32 v[166:167], v147 offset0:199 offset1:215
	v_mul_f32_e32 v146, 0x42000000, v154
	v_med3_f32 v0, v146, s41, v143
	v_cvt_pk_fp8_f32 v150, v0, v2 op_sel:[0,0,1]
	s_waitcnt lgkmcnt(3)
	v_mul_f32_e32 v0, 0x42000000, v160
	s_waitcnt lgkmcnt(2)
	v_mul_f32_e32 v2, 0x42000000, v162
	s_waitcnt lgkmcnt(0)
	v_mul_f32_e32 v148, 0x42000000, v166
	v_med3_f32 v0, v0, s41, v143
	v_med3_f32 v2, v2, s41, v143
	v_mov_b32_e32 v151, 0
	v_cvt_pk_fp8_f32 v151, v0, v2
	v_med3_f32 v2, v148, s41, v143
	v_add_u32_e32 v148, 0x800, v142
	ds_read2_b32 v[168:169], v148 offset0:8 offset1:24
	ds_read2_b32 v[170:171], v148 offset0:73 offset1:89
	ds_read2_b32 v[172:173], v148 offset0:138 offset1:154
	ds_read2_b32 v[174:175], v148 offset0:203 offset1:219
	v_mul_f32_e32 v146, 0x42000000, v164
	v_med3_f32 v0, v146, s41, v143
	v_cvt_pk_fp8_f32 v151, v0, v2 op_sel:[0,0,1]
	s_waitcnt lgkmcnt(3)
	v_mul_f32_e32 v0, 0x42000000, v168
	s_waitcnt lgkmcnt(2)
	v_mul_f32_e32 v2, 0x42000000, v170
	s_waitcnt lgkmcnt(1)
	v_mul_f32_e32 v146, 0x42000000, v172
	v_med3_f32 v0, v0, s41, v143
	v_med3_f32 v2, v2, s41, v143
	v_mov_b32_e32 v152, 0
	v_cvt_pk_fp8_f32 v152, v0, v2
	v_med3_f32 v0, v146, s41, v143
	v_add_u32_e32 v146, 0xc00, v142
	ds_read2_b32 v[176:177], v146 offset0:12 offset1:28
	ds_read2_b32 v[178:179], v146 offset0:77 offset1:93
	ds_read2_b32 v[180:181], v146 offset0:142 offset1:158
	s_waitcnt lgkmcnt(3)
	v_mul_f32_e32 v153, 0x42000000, v174
	v_med3_f32 v2, v153, s41, v143
	ds_read2_b32 v[182:183], v146 offset0:207 offset1:223
	v_cvt_pk_fp8_f32 v152, v0, v2 op_sel:[0,0,1]
	s_waitcnt lgkmcnt(3)
	v_mul_f32_e32 v0, 0x42000000, v176
	s_waitcnt lgkmcnt(2)
	v_mul_f32_e32 v2, 0x42000000, v178
	v_med3_f32 v0, v0, s41, v143
	v_med3_f32 v2, v2, s41, v143
	v_mov_b32_e32 v153, 0
	v_cvt_pk_fp8_f32 v153, v0, v2
	s_waitcnt lgkmcnt(1)
	v_mul_f32_e32 v154, 0x42000000, v180
	s_waitcnt lgkmcnt(0)
; #define LAS __attribute__((address_space(3)))
; #define GAS __attribute__((address_space(1)))
; __device__ __forceinline__ unsigned pk_fp8x4(float a, float b, float c, float d) { int p = __builtin_amdgcn_cvt_pk_fp8_f32(sat8(a), sat8(b), 0, false); p = __builtin_amdgcn_cvt_pk_fp8_f32(sat8(c), sat8(d), p, true); return (unsigned)p; }
; __device__ __forceinline__ void tr_finish(const TrDesc& d, f32x4 (&v)[16], LAS float* scr, int lane) {
;     ...
;         const int c = lane & 3, nl = lane >> 2; const LAS float* sp = scr + (16 * c) * 65 + nl; unsigned char* dp = d.dst + (size_t)nl * d.K + 16 * c;
; #pragma unroll
;         for (int j = 0; j < 4; ++j) { u32x4 o;
;             o.x = pk_fp8x4(sp[0 * 65 + 16 * j] * 32.0f, sp[1 * 65 + 16 * j] * 32.0f, sp[2 * 65 + 16 * j] * 32.0f, sp[3 * 65 + 16 * j] * 32.0f);
;             o.y = pk_fp8x4(sp[4 * 65 + 16 * j] * 32.0f, sp[5 * 65 + 16 * j] * 32.0f, sp[6 * 65 + 16 * j] * 32.0f, sp[7 * 65 + 16 * j] * 32.0f);
;             o.z = pk_fp8x4(sp[8 * 65 + 16 * j] * 32.0f, sp[9 * 65 + 16 * j] * 32.0f, sp[10 * 65 + 16 * j] * 32.0f, sp[11 * 65 + 16 * j] * 32.0f);
;             o.w = pk_fp8x4(sp[12 * 65 + 16 * j] * 32.0f, sp[13 * 65 + 16 * j] * 32.0f, sp[14 * 65 + 16 * j] * 32.0f, sp[15 * 65 + 16 * j] * 32.0f);
;             *(GAS u32x4*)(dp + (size_t)(16 * j) * d.K) = o; }
;     ...
;         while (it < NIT) {
;             const int itB = it + NGW;
;             if (itB < NIT) { dB = decode(NIT - 1 - itB); tr_load(dB, vB); }
;             tr_finish(dA, vA, scr, lane);
;             if (itB >= NIT) break;
;             const int itA = itB + NGW;
;             if (itA < NIT) { dA = decode(NIT - 1 - itA); tr_load(dA, vA); }
;             tr_finish(dB, vB, scr, lane);
;             it = itA;
	v_mul_f32_e32 v0, 0x42000000, v182
	v_med3_f32 v2, v154, s41, v143
	v_med3_f32 v0, v0, s41, v143
	v_cvt_pk_fp8_f32 v153, v2, v0 op_sel:[0,0,1]
	v_mov_b64_e32 v[158:159], s[16:17]
	v_mad_i64_i32 v[158:159], s[22:23], s2, v132, v[158:159]
	v_lshl_add_u64 v[158:159], v[158:159], 0, v[134:135]
	v_mul_f32_e32 v0, 0x42000000, v3
	v_mul_f32_e32 v2, 0x42000000, v149
	global_store_dwordx4 v[158:159], v[150:153], off
	v_med3_f32 v0, v0, s41, v143
	v_med3_f32 v2, v2, s41, v143
	v_mov_b32_e32 v150, 0
	v_cvt_pk_fp8_f32 v150, v0, v2
	v_mul_f32_e32 v3, 0x42000000, v155
	v_mul_f32_e32 v0, 0x42000000, v157
	v_med3_f32 v2, v3, s41, v143
	v_med3_f32 v0, v0, s41, v143
	v_cvt_pk_fp8_f32 v150, v2, v0 op_sel:[0,0,1]
	v_mul_f32_e32 v0, 0x42000000, v161
	v_mul_f32_e32 v2, 0x42000000, v163
	v_med3_f32 v0, v0, s41, v143
	v_med3_f32 v2, v2, s41, v143
	v_mov_b32_e32 v151, 0
	v_cvt_pk_fp8_f32 v151, v0, v2
	v_mul_f32_e32 v3, 0x42000000, v165
	v_mul_f32_e32 v0, 0x42000000, v167
	v_med3_f32 v2, v3, s41, v143
	v_med3_f32 v0, v0, s41, v143
	v_cvt_pk_fp8_f32 v151, v2, v0 op_sel:[0,0,1]
	v_mul_f32_e32 v0, 0x42000000, v169
	v_mul_f32_e32 v2, 0x42000000, v171
	v_med3_f32 v0, v0, s41, v143
	v_med3_f32 v2, v2, s41, v143
	v_mov_b32_e32 v152, 0
	v_cvt_pk_fp8_f32 v152, v0, v2
	v_mul_f32_e32 v3, 0x42000000, v173
	v_mul_f32_e32 v0, 0x42000000, v175
	v_med3_f32 v2, v3, s41, v143
	v_med3_f32 v0, v0, s41, v143
	v_cvt_pk_fp8_f32 v152, v2, v0 op_sel:[0,0,1]
	v_mul_f32_e32 v0, 0x42000000, v177
	v_mul_f32_e32 v2, 0x42000000, v179
	v_med3_f32 v0, v0, s41, v143
	v_med3_f32 v2, v2, s41, v143
	v_mov_b32_e32 v153, 0
	v_cvt_pk_fp8_f32 v153, v0, v2
	s_ashr_i32 s3, s2, 31
	v_mul_f32_e32 v3, 0x42000000, v181
	v_mul_f32_e32 v0, 0x42000000, v183
	v_med3_f32 v2, v3, s41, v143
	v_med3_f32 v0, v0, s41, v143
	s_lshl_b64 s[22:23], s[2:3], 4
	v_cvt_pk_fp8_f32 v153, v2, v0 op_sel:[0,0,1]
	v_lshl_add_u64 v[2:3], v[158:159], 0, s[22:23]
	ds_read2_b32 v[154:155], v142 offset0:32 offset1:48
	ds_read2_b32 v[156:157], v142 offset0:97 offset1:113
	ds_read2_b32 v[158:159], v142 offset0:162 offset1:178
	ds_read2_b32 v[160:161], v142 offset0:227 offset1:243
	s_andn2_b64 vcc, exec, s[20:21]
	s_waitcnt lgkmcnt(3)
	v_mul_f32_e32 v0, 0x42000000, v154
	s_waitcnt lgkmcnt(2)
	v_mul_f32_e32 v149, 0x42000000, v156
	global_store_dwordx4 v[2:3], v[150:153], off
	v_med3_f32 v0, v0, s41, v143
	v_med3_f32 v149, v149, s41, v143
	v_mov_b32_e32 v150, 0
	v_cvt_pk_fp8_f32 v150, v0, v149
	ds_read2_b32 v[162:163], v147 offset0:36 offset1:52
	ds_read2_b32 v[164:165], v147 offset0:101 offset1:117
	ds_read2_b32 v[166:167], v147 offset0:166 offset1:182
	ds_read2_b32 v[168:169], v147 offset0:231 offset1:247
	s_waitcnt lgkmcnt(5)
	v_mul_f32_e32 v151, 0x42000000, v158
	s_waitcnt lgkmcnt(4)
	v_mul_f32_e32 v152, 0x42000000, v160
	v_med3_f32 v0, v151, s41, v143
	v_med3_f32 v149, v152, s41, v143
	v_cvt_pk_fp8_f32 v150, v0, v149 op_sel:[0,0,1]
	s_waitcnt lgkmcnt(3)
	v_mul_f32_e32 v0, 0x42000000, v162
	s_waitcnt lgkmcnt(2)
	v_mul_f32_e32 v149, 0x42000000, v164
	v_med3_f32 v0, v0, s41, v143
	v_med3_f32 v149, v149, s41, v143
	v_mov_b32_e32 v151, 0
	v_cvt_pk_fp8_f32 v151, v0, v149
	ds_read2_b32 v[170:171], v148 offset0:40 offset1:56
	ds_read2_b32 v[172:173], v148 offset0:105 offset1:121
	ds_read2_b32 v[174:175], v148 offset0:170 offset1:186
	ds_read2_b32 v[176:177], v148 offset0:235 offset1:251
	s_waitcnt lgkmcnt(5)
	v_mul_f32_e32 v152, 0x42000000, v166
	s_waitcnt lgkmcnt(4)
	v_mul_f32_e32 v153, 0x42000000, v168
	v_med3_f32 v0, v152, s41, v143
	v_med3_f32 v149, v153, s41, v143
	v_cvt_pk_fp8_f32 v151, v0, v149 op_sel:[0,0,1]
	s_waitcnt lgkmcnt(3)
	v_mul_f32_e32 v0, 0x42000000, v170
	s_waitcnt lgkmcnt(2)
	v_mul_f32_e32 v149, 0x42000000, v172
	v_med3_f32 v0, v0, s41, v143
	v_med3_f32 v149, v149, s41, v143
	v_mov_b32_e32 v152, 0
	v_cvt_pk_fp8_f32 v152, v0, v149
	ds_read2_b32 v[178:179], v146 offset0:44 offset1:60
	ds_read2_b32 v[180:181], v146 offset0:109 offset1:125
	ds_read2_b32 v[182:183], v146 offset0:174 offset1:190
	s_waitcnt lgkmcnt(4)
	v_mul_f32_e32 v153, 0x42000000, v174
	s_waitcnt lgkmcnt(3)
	v_mul_f32_e32 v154, 0x42000000, v176
	v_med3_f32 v0, v153, s41, v143
	v_med3_f32 v149, v154, s41, v143
	ds_read2_b32 v[184:185], v146 offset0:239 offset1:255
	v_cvt_pk_fp8_f32 v152, v0, v149 op_sel:[0,0,1]
	s_waitcnt lgkmcnt(3)
	v_mul_f32_e32 v0, 0x42000000, v178
	s_waitcnt lgkmcnt(2)
	v_mul_f32_e32 v149, 0x42000000, v180
	v_med3_f32 v0, v0, s41, v143
	v_med3_f32 v149, v149, s41, v143
	v_mov_b32_e32 v153, 0
	v_cvt_pk_fp8_f32 v153, v0, v149
	s_waitcnt lgkmcnt(1)
	v_mul_f32_e32 v154, 0x42000000, v182
	s_waitcnt lgkmcnt(0)
	v_mul_f32_e32 v0, 0x42000000, v184
	v_med3_f32 v149, v154, s41, v143
	v_med3_f32 v0, v0, s41, v143
	v_cvt_pk_fp8_f32 v153, v149, v0 op_sel:[0,0,1]
	v_mul_f32_e32 v0, 0x42000000, v155
	v_mul_f32_e32 v149, 0x42000000, v157
	v_med3_f32 v0, v0, s41, v143
	v_med3_f32 v149, v149, s41, v143
	v_mov_b32_e32 v154, 0
	v_cvt_pk_fp8_f32 v154, v0, v149
	v_mul_f32_e32 v155, 0x42000000, v159
	v_mul_f32_e32 v0, 0x42000000, v161
	v_med3_f32 v149, v155, s41, v143
	v_med3_f32 v0, v0, s41, v143
	v_cvt_pk_fp8_f32 v154, v149, v0 op_sel:[0,0,1]
	v_mul_f32_e32 v0, 0x42000000, v163
	v_mul_f32_e32 v149, 0x42000000, v165
	v_med3_f32 v0, v0, s41, v143
	v_med3_f32 v149, v149, s41, v143
	v_mov_b32_e32 v155, 0
	v_cvt_pk_fp8_f32 v155, v0, v149
	v_mul_f32_e32 v156, 0x42000000, v167
	v_mul_f32_e32 v0, 0x42000000, v169
	v_med3_f32 v149, v156, s41, v143
	v_med3_f32 v0, v0, s41, v143
	v_cvt_pk_fp8_f32 v155, v149, v0 op_sel:[0,0,1]
	v_mul_f32_e32 v0, 0x42000000, v171
	v_mul_f32_e32 v149, 0x42000000, v173
	v_med3_f32 v0, v0, s41, v143
	v_med3_f32 v149, v149, s41, v143
	v_mov_b32_e32 v156, 0
	v_cvt_pk_fp8_f32 v156, v0, v149
	v_mul_f32_e32 v157, 0x42000000, v175
	v_mul_f32_e32 v0, 0x42000000, v177
	v_med3_f32 v149, v157, s41, v143
	v_med3_f32 v0, v0, s41, v143
	v_cvt_pk_fp8_f32 v156, v149, v0 op_sel:[0,0,1]
	v_mul_f32_e32 v0, 0x42000000, v179
	v_mul_f32_e32 v149, 0x42000000, v181
	v_med3_f32 v0, v0, s41, v143
	v_med3_f32 v149, v149, s41, v143
	v_mov_b32_e32 v157, 0
	v_cvt_pk_fp8_f32 v157, v0, v149
	v_mul_f32_e32 v158, 0x42000000, v183
	v_mul_f32_e32 v0, 0x42000000, v185
	v_med3_f32 v149, v158, s41, v143
	v_med3_f32 v0, v0, s41, v143
	v_cvt_pk_fp8_f32 v157, v149, v0 op_sel:[0,0,1]
	v_lshl_add_u64 v[2:3], v[2:3], 0, s[22:23]
	global_store_dwordx4 v[2:3], v[150:153], off
	v_lshl_add_u64 v[2:3], v[2:3], 0, s[22:23]
	global_store_dwordx4 v[2:3], v[154:157], off
	s_waitcnt lgkmcnt(0)
	s_cbranch_vccnz .LBB0_71
	s_add_i32 s42, s44, s48
	s_cmp_lt_i32 s42, 0x800
	s_cbranch_scc1 .Lpt_2
	s_cmp_ge_i32 s42, 0xc880
	s_cbranch_scc1 .Lpt_2
	s_add_i32 s42, s42, 0xc080

;     ...
;         const int gw = vcu * NWAVES + wave, NGW = G * NWAVES;
;         constexpr int C_IN = 32 * 188, C_OA = 8 * 32, C_OB = 16 * 32, C_O = 32 * 32, C_GU = 16 * 32 * 32, C_DN = 16 * 16 * 32, C_L = C_IN + C_OA + C_OB + C_O + C_GU + C_DN, NIT = DEPTH * C_L;
;         const int q4 = lane & 15, kk = lane >> 4;
;         auto decode = [&](int it) -> TrDesc {
;             TrDesc d; d.zero = 0; d.rope = 0; d.f8 = 0;
;             const int l = it / C_L; int r = it % C_L;
;             const float* W; unsigned char* WT; int ldw, K, k0, n0, scol, esz = 2;
;             if (r < C_IN) { const int kb = r / 188, nb = r % 188; n0 = 64 * nb; k0 = 64 * kb; ldw = NIN; K = D; W = a.w_in + (size_t)l * D * NIN;
;                 if (n0 < 3072) { d.rope = 1; scol = (n0 >> 7) * 128 + 32 * ((n0 >> 6) & 1) + 64 * (q4 >> 3) + 4 * (q4 & 7); }
;                 else if (n0 < 7680) scol = n0 + 4 * q4;
;                 else if (n0 < 11776) scol = n0 + 16 + 4 * q4;
;                 else if (n0 == 11776) { scol = (q4 < 4) ? 7680 + 4 * q4 : 0; d.zero = (q4 < 4) ? 0 : 1; }
;                 else { scol = 0; d.zero = 1; }
;     ...
;                 d.f8 = 1; esz = 1; WT = ws + WS_WIN + (size_t)l * NP * D;
;     ...
;                 WT = ws + WS_WIN + (size_t)l * NP * D * 2;
;     ...
;             } else if ((r -= C_IN) < C_OA) { const int kb = r / 32, nb = r % 32; n0 = 64 * nb; k0 = 64 * kb; ldw = D; K = 512; scol = n0 + 4 * q4; W = a.w_out_a + (size_t)l * 512 * D; WT = ws + WS_WOA + (size_t)l * D * 512 * (MIX_F8 ? 1 : 2); if (MIX_F8) { d.f8 = 1; esz = 1; }
;                 if (BR_FUSE) { K = 1536; WT = ws + WS_WOA + (size_t)l * D * 1536 + 1024; }
;             } else if ((r -= C_OA) < C_OB) { const int kb = r / 32, nb = r % 32; n0 = 64 * nb; k0 = 64 * kb; ldw = D; K = 1024; scol = n0 + 4 * q4; W = a.w_out_b + (size_t)l * 1024 * D; WT = ws + WS_WOB + (size_t)l * D * 1024 * (MIX_F8 ? 1 : 2); if (MIX_F8) { d.f8 = 1; esz = 1; }
; template <unsigned MASK, bool ONE>
; __global__ void __launch_bounds__(NTHREADS, 2) fwd_kernel(Args a_unused) {
;     ...
;         if (IN(P + 1, 2)) { FRESH_TID();
;     ...
;             pg8::StaticOrderP S{T / 256, NP / 256, G, bx}; pg8::RowsContig AM; pg8::EpiProj E{proj, ropec, ropes, alow, pg8::W8_INV};
;             pg8::gemm_phase<pg8::EpiProj, pg8::StaticOrderP, pg8::RowsContig, true, true>(lds, tid, hbuf, (const bf16_t*)(ws + WS_WIN + (size_t)l * NP * D), 0, D / 2, S, AM, E);
.LBB0_265:
	s_or_b64 exec, exec, s[0:1]
	v_readlane_b32 s0, v253, 0
	v_readlane_b32 s1, v253, 1
	s_mov_b32 s2, s38
	s_waitcnt lgkmcnt(0)
	s_barrier
	s_nop 0
	v_mbcnt_lo_u32_b32 v0, s2, 0
	v_mbcnt_hi_u32_b32 v0, s2, v0
	v_readlane_b32 s2, v253, 7
	v_readlane_b32 s3, v253, 8
	v_add_u32_e32 v1, s78, v0
	s_andn2_b64 vcc, exec, s[2:3]
	v_readfirstlane_b32 s16, v1
	v_readlane_b32 s101, v255, 17
	s_movk_i32 s100, 0x100
	s_cmp_eq_u32 s101, 0
	s_cbranch_scc0 .Lpq_skip
	s_movk_i32 s100, 0xe8
	v_readlane_b32 s101, v253, 4
	s_nop 1
	s_cmp_lt_i32 s101, s100
	s_cbranch_scc1 .Lpq_skip
	s_mov_b32 s100, 0x9e80
	s_mov_b32 s101, 0xc880
	v_writelane_b32 v251, s16, 0
	v_writelane_b32 v251, s17, 1
	v_writelane_b32 v251, s18, 2
	v_writelane_b32 v251, s19, 3
	v_writelane_b32 v251, s20, 4
	v_writelane_b32 v251, s21, 5
	v_writelane_b32 v251, s23, 6
	v_writelane_b32 v251, s25, 7
	v_writelane_b32 v251, s26, 8
	v_writelane_b32 v251, s33, 9
	v_writelane_b32 v251, s38, 10
	v_writelane_b32 v251, s39, 11
	v_writelane_b32 v251, s41, 12
	v_writelane_b32 v251, s42, 13
	v_writelane_b32 v251, s45, 14
	v_writelane_b32 v251, s48, 15
	v_writelane_b32 v251, s49, 16
	v_writelane_b32 v251, s50, 17
	v_writelane_b32 v251, s51, 18
	v_writelane_b32 v251, s74, 19
	v_writelane_b32 v251, s76, 20
	v_mov_b32_e32 v193, v3
	v_mov_b32_e32 v194, v33
	v_mov_b32_e32 v195, v59
	v_mov_b32_e32 v196, v63
	v_mov_b32_e32 v197, v110
	v_mov_b32_e32 v198, v111
	v_mov_b32_e32 v199, v114
	v_mov_b32_e32 v200, v115
	v_mov_b32_e32 v201, v149
	v_mov_b32_e32 v202, v153
	v_mov_b32_e32 v203, v157
	v_mov_b32_e32 v204, v161
	v_mov_b32_e32 v205, v165
	v_mov_b32_e32 v206, v169
	v_mov_b32_e32 v207, v173
	v_mov_b32_e32 v208, v177
	v_mov_b32_e32 v209, v178
	v_mov_b32_e32 v210, v179
	v_mov_b32_e32 v211, v180
	v_mov_b32_e32 v212, v181
	v_mov_b32_e32 v214, v182
	v_mov_b32_e32 v215, v183
	v_mov_b32_e32 v216, v184
	v_mov_b32_e32 v218, v185
	v_readlane_b32 s76, v253, 4
	v_readlane_b32 s8, v253, 0
	v_readlane_b32 s9, v253, 1
	s_nop 1
	s_sub_i32 s0, s76, 232
	s_lshr_b32 s1, s100, 3
	s_add_i32 s0, s0, s1
	s_lshr_b32 s33, s78, 6
	s_lshr_b32 s1, s0, 3
	s_lshl_b32 s1, s1, 6
	s_and_b32 s0, s0, 7
	s_lshl_b32 s0, s0, 2
	s_or_b32 s1, s1, s0
	s_and_b32 s0, s33, 3
	s_or_b32 s1, s1, s0
	s_lshr_b32 s0, s33, 2
	s_lshl_b32 s0, s0, 5
	s_or_b32 s1, s1, s0
	s_sub_i32 s100, s1, s33
	s_mov_b32 s76, 0
	s_movk_i32 s74, 24
	s_load_dwordx2 s[10:11], s[8:9], 0xa0
	v_mbcnt_lo_u32_b32 v69, -1, 0
	v_mbcnt_hi_u32_b32 v69, -1, v69
	s_mov_b64 exec, -1
	v_lshlrev_b32_e32 v76, 3, v69
	s_waitcnt lgkmcnt(0)
	s_lshl_b32 s47, s76, 3
	s_add_i32 s47, s47, s33
	s_add_i32 s47, s47, s100
	v_and_b32_e32 v2, 15, v69
	s_cmp_ge_i32 s47, s101
	v_ashrrev_i32_e32 v133, 4, v69
	s_cbranch_scc1 .LBB0_36_hq
	s_sub_i32 s1, 0xfcff, s47
	s_mul_hi_u32 s0, s1, 0x81848da9
	s_lshr_b32 s0, s0, 14
	s_mul_i32 s2, s0, 0x7e80
	s_sub_i32 s17, s1, s2
	s_cmpk_gt_u32 s17, 0x177f
	s_cbranch_scc0 .LBB0_37_hq
	s_cmpk_gt_u32 s17, 0x187f
	s_cbranch_scc0 .LBB0_39_hq
	s_cmpk_gt_u32 s17, 0x1a7f
	s_cbranch_scc0 .LBB0_40_hq
	s_cmpk_gt_u32 s17, 0x1e7f
	s_cbranch_scc0 .LBB0_41_hq
	s_lshl_b32 s1, s17, 6
	s_cmpk_gt_u32 s17, 0x5e7f
	s_cbranch_scc0 .LBB0_42_hq
	s_add_i32 s2, s17, 0xffffa180
	s_lshr_b32 s4, s2, 9
	s_lshl_b32 s2, s2, 1
	s_and_b32 s18, s2, 0x3c0
	s_load_dwordx2 s[2:3], s[8:9], 0x88
	s_lshl_b32 s5, s0, 4
	s_add_i32 s6, s4, s5
	s_mov_b32 s7, 0
	s_and_b32 s16, s1, 0x7c0
	s_lshl_b64 s[4:5], s[6:7], 23
	s_waitcnt lgkmcnt(0)
	s_add_u32 s4, s2, s4
	s_addc_u32 s5, s3, s5
	s_lshl_b64 s[2:3], s[6:7], 21
	s_add_u32 s2, s10, s2
	s_addc_u32 s3, s11, s3
	s_add_u32 s6, s2, 0x18600000
	v_lshl_or_b32 v0, v2, 2, s16
	s_addc_u32 s7, s3, 0
	s_mov_b64 s[2:3], 0
	s_branch .LBB0_43_hq

;     ...
;         auto decode = [&](int it) -> TrDesc {
;             TrDesc d; d.zero = 0; d.rope = 0; d.f8 = 0;
;             const int l = it / C_L; int r = it % C_L;
;             const float* W; unsigned char* WT; int ldw, K, k0, n0, scol, esz = 2;
;             if (r < C_IN) { const int kb = r / 188, nb = r % 188; n0 = 64 * nb; k0 = 64 * kb; ldw = NIN; K = D; W = a.w_in + (size_t)l * D * NIN;
;                 if (n0 < 3072) { d.rope = 1; scol = (n0 >> 7) * 128 + 32 * ((n0 >> 6) & 1) + 64 * (q4 >> 3) + 4 * (q4 & 7); }
;                 else if (n0 < 7680) scol = n0 + 4 * q4;
;                 else if (n0 < 11776) scol = n0 + 16 + 4 * q4;
;                 else if (n0 == 11776) { scol = (q4 < 4) ? 7680 + 4 * q4 : 0; d.zero = (q4 < 4) ? 0 : 1; }
;                 else { scol = 0; d.zero = 1; }
;     ...
;                 d.f8 = 1; esz = 1; WT = ws + WS_WIN + (size_t)l * NP * D;
;     ...
;                 WT = ws + WS_WIN + (size_t)l * NP * D * 2;
;     ...
;             } else if ((r -= C_IN) < C_OA) { const int kb = r / 32, nb = r % 32; n0 = 64 * nb; k0 = 64 * kb; ldw = D; K = 512; scol = n0 + 4 * q4; W = a.w_out_a + (size_t)l * 512 * D; WT = ws + WS_WOA + (size_t)l * D * 512 * (MIX_F8 ? 1 : 2); if (MIX_F8) { d.f8 = 1; esz = 1; }
;                 if (BR_FUSE) { K = 1536; WT = ws + WS_WOA + (size_t)l * D * 1536 + 1024; }
;             } else if ((r -= C_OA) < C_OB) { const int kb = r / 32, nb = r % 32; n0 = 64 * nb; k0 = 64 * kb; ldw = D; K = 1024; scol = n0 + 4 * q4; W = a.w_out_b + (size_t)l * 1024 * D; WT = ws + WS_WOB + (size_t)l * D * 1024 * (MIX_F8 ? 1 : 2); if (MIX_F8) { d.f8 = 1; esz = 1; }
;                 if (BR_FUSE) { K = 1536; WT = ws + WS_WOA + (size_t)l * D * 1536; }
;             } else if ((r -= C_OB) < C_O) { const int kb = r / 32, nb = r % 32; n0 = 64 * nb; k0 = 64 * kb; ldw = D; K = D; scol = n0 + 4 * q4; W = a.w_out + (size_t)l * D * D; WT = ws + WS_WO + (size_t)l * D * D * (MIX_F8 ? 1 : 2); if (MIX_F8) { d.f8 = 1; esz = 1; }
;     ...
;         while (it < NIT) {
;             const int itB = it + NGW;
;             if (itB < NIT) { dB = decode(NIT - 1 - itB); tr_load(dB, vB); }
;             tr_finish(dA, vA, scr, lane);
;             if (itB >= NIT) break;
;             const int itA = itB + NGW;
;             if (itA < NIT) { dA = decode(NIT - 1 - itA); tr_load(dA, vA); }
.LBB0_72_hq:
	s_cmp_ge_i32 s42, s101
	s_cbranch_scc1 .LBB0_70_hq
	s_lshr_b32 s44, s42, 6
	s_lshl_b32 s44, s44, 3
	s_bfe_u32 s100, s42, 0x30002
	s_or_b32 s44, s44, s100
	s_add_i32 s44, s44, 24
	s_and_b32 s100, s44, 7
	s_lshr_b32 s44, s44, 3
	s_lshl_b32 s44, s44, 6
	s_lshl_b32 s100, s100, 2
	s_or_b32 s44, s44, s100
	s_and_b32 s100, s42, 0x23
	s_or_b32 s44, s44, s100
	s_cmp_lt_i32 s44, s101
	s_cselect_b64 s[20:21], -1, 0
	s_cmp_ge_i32 s44, s101
	s_cselect_b64 s[12:13], -1, 0
	s_and_b64 vcc, exec, s[12:13]
	s_cbranch_vccnz .LBB0_106_hq
	s_sub_i32 s3, 0xfcff, s44
	s_mul_hi_u32 s0, s3, 0x81848da9
	s_lshr_b32 s0, s0, 14
	s_mul_i32 s14, s0, 0x7e80
	s_sub_i32 s45, s3, s14
	s_cmpk_gt_u32 s45, 0x177f
	s_cbranch_scc0 .LBB0_81_hq
	s_cmpk_gt_u32 s45, 0x187f
	s_cbranch_scc0 .LBB0_83_hq
	s_cmpk_gt_u32 s45, 0x1a7f
	s_cbranch_scc0 .LBB0_84_hq
	s_cmpk_gt_u32 s45, 0x1e7f
	s_cbranch_scc0 .LBB0_85_hq
	s_lshl_b32 s24, s45, 6
	s_cmpk_gt_u32 s45, 0x5e7f
	s_cbranch_scc0 .LBB0_121_hq
	s_add_i32 s14, s45, 0xffffa180
	s_lshr_b32 s18, s14, 9
	s_lshl_b32 s14, s14, 1
	s_and_b32 s49, s14, 0x3c0
	s_load_dwordx2 s[14:15], s[8:9], 0x88
	s_lshl_b32 s19, s0, 4
	s_add_i32 s22, s18, s19
	s_mov_b32 s23, s1
	s_and_b32 s3, s24, 0x7c0
	s_lshl_b64 s[18:19], s[22:23], 23
	s_waitcnt lgkmcnt(0)
	s_add_u32 s18, s14, s18
	s_addc_u32 s19, s15, s19
	s_lshl_b64 s[14:15], s[22:23], 21
	s_add_u32 s22, s28, s14
	v_or_b32_e32 v0, s3, v136
	s_addc_u32 s23, s29, s15
	s_cbranch_execz .LBB0_122_hq
	s_movk_i32 s14, 0x400
	s_mov_b64 s[24:25], 0x800
	s_cbranch_execz .LBB0_86_hq
	s_branch .LBB0_87_hq

; #define LAS __attribute__((address_space(3)))
; #define LDS_WAIT() asm volatile("s_waitcnt lgkmcnt(0)" ::: "memory")
; __device__ __forceinline__ unsigned pk_fp8x4(float a, float b, float c, float d) { int p = __builtin_amdgcn_cvt_pk_fp8_f32(sat8(a), sat8(b), 0, false); p = __builtin_amdgcn_cvt_pk_fp8_f32(sat8(c), sat8(d), p, true); return (unsigned)p; }
; __device__ __forceinline__ void tr_finish(const TrDesc& d, f32x4 (&v)[16], LAS float* scr, int lane) {
;     ...
;     const int d0 = d.rope ? 8 * (q4 & 7) + (q4 >> 3) : 4 * q4, ds = d.rope ? 2 : 1;
;     { LAS float* rp = scr + kk * 65 + d0;
; #pragma unroll
;         for (int i = 0; i < 16; ++i) { rp[4 * i * 65] = v[i][0]; rp[4 * i * 65 + ds] = v[i][1]; rp[4 * i * 65 + 2 * ds] = v[i][2]; rp[4 * i * 65 + 3 * ds] = v[i][3]; } }
;     LDS_WAIT(); asm volatile("" ::: "memory");
;     if (d.f8) {
;         const int c = lane & 3, nl = lane >> 2; const LAS float* sp = scr + (16 * c) * 65 + nl; unsigned char* dp = d.dst + (size_t)nl * d.K + 16 * c;
; #pragma unroll
;         for (int j = 0; j < 4; ++j) { u32x4 o;
;             o.x = pk_fp8x4(sp[0 * 65 + 16 * j] * 32.0f, sp[1 * 65 + 16 * j] * 32.0f, sp[2 * 65 + 16 * j] * 32.0f, sp[3 * 65 + 16 * j] * 32.0f);
;             o.y = pk_fp8x4(sp[4 * 65 + 16 * j] * 32.0f, sp[5 * 65 + 16 * j] * 32.0f, sp[6 * 65 + 16 * j] * 32.0f, sp[7 * 65 + 16 * j] * 32.0f);
;             o.z = pk_fp8x4(sp[8 * 65 + 16 * j] * 32.0f, sp[9 * 65 + 16 * j] * 32.0f, sp[10 * 65 + 16 * j] * 32.0f, sp[11 * 65 + 16 * j] * 32.0f);
;             o.w = pk_fp8x4(sp[12 * 65 + 16 * j] * 32.0f, sp[13 * 65 + 16 * j] * 32.0f, sp[14 * 65 + 16 * j] * 32.0f, sp[15 * 65 + 16 * j] * 32.0f);
.LBB0_108_hq:
	s_or_b64 exec, exec, s[22:23]
	s_cmp_eq_u32 s43, 0
	s_cselect_b64 vcc, -1, 0
	s_cmp_lg_u32 s43, 0
	s_cselect_b64 s[22:23], -1, 0
	v_cndmask_b32_e64 v2, 0, 1, s[22:23]
	s_and_b64 s[22:23], s[22:23], exec
	v_cndmask_b32_e32 v0, v140, v136, vcc
	s_cselect_b32 s0, 2, 1
	v_lshl_add_u32 v0, v0, 2, v141
	s_lshl_b32 s3, s0, 2
	v_add_u32_e32 v3, s3, v0
	v_lshlrev_b32_e64 v2, v2, 3
	s_waitcnt vmcnt(15)
	ds_write_b32 v3, v5
	v_lshl_add_u32 v3, s0, 3, v0
	v_lshl_add_u32 v2, v2, 2, v0
	v_subrev_u32_e32 v146, s3, v3
	ds_write_b32 v0, v4
	ds_write_b32 v3, v6
	ds_write_b32 v2, v7
	s_waitcnt vmcnt(14)
	ds_write_b32 v0, v8 offset:1040
	ds_write_b32 v146, v9 offset:1040
	ds_write_b32 v3, v10 offset:1040
	ds_write_b32 v2, v11 offset:1040
	s_waitcnt vmcnt(13)
	ds_write_b32 v0, v12 offset:2080
	ds_write_b32 v146, v13 offset:2080
	ds_write_b32 v3, v14 offset:2080
	ds_write_b32 v2, v15 offset:2080
	s_waitcnt vmcnt(12)
	ds_write_b32 v0, v16 offset:3120
	ds_write_b32 v146, v17 offset:3120
	ds_write_b32 v3, v18 offset:3120
	ds_write_b32 v2, v19 offset:3120
	s_waitcnt vmcnt(11)
	ds_write_b32 v0, v20 offset:4160
	ds_write_b32 v146, v21 offset:4160
	ds_write_b32 v3, v22 offset:4160
	ds_write_b32 v2, v23 offset:4160
	s_waitcnt vmcnt(10)
	ds_write_b32 v0, v24 offset:5200
	ds_write_b32 v146, v25 offset:5200
	ds_write_b32 v3, v26 offset:5200
	ds_write_b32 v2, v27 offset:5200
	s_waitcnt vmcnt(9)
	ds_write_b32 v0, v28 offset:6240
	ds_write_b32 v146, v29 offset:6240
	ds_write_b32 v3, v30 offset:6240
	ds_write_b32 v2, v31 offset:6240
	s_waitcnt vmcnt(8)
	ds_write_b32 v0, v32 offset:7280
	ds_write_b32 v146, v33 offset:7280
	ds_write_b32 v3, v34 offset:7280
	ds_write_b32 v2, v35 offset:7280
	s_waitcnt vmcnt(7)
	ds_write_b32 v0, v36 offset:8320
	ds_write_b32 v146, v37 offset:8320
	ds_write_b32 v3, v38 offset:8320
	ds_write_b32 v2, v39 offset:8320
	s_waitcnt vmcnt(6)
	ds_write_b32 v0, v40 offset:9360
	ds_write_b32 v146, v41 offset:9360
	ds_write_b32 v3, v42 offset:9360
	ds_write_b32 v2, v43 offset:9360
	s_waitcnt vmcnt(5)
	ds_write_b32 v0, v44 offset:10400
	ds_write_b32 v146, v45 offset:10400
	ds_write_b32 v3, v46 offset:10400
	ds_write_b32 v2, v47 offset:10400
	s_waitcnt vmcnt(4)
	ds_write_b32 v0, v48 offset:11440
	ds_write_b32 v146, v49 offset:11440
	ds_write_b32 v3, v50 offset:11440
	ds_write_b32 v2, v51 offset:11440
	s_waitcnt vmcnt(3)
	ds_write_b32 v0, v52 offset:12480
	ds_write_b32 v146, v53 offset:12480
	ds_write_b32 v3, v54 offset:12480
	ds_write_b32 v2, v55 offset:12480
	s_waitcnt vmcnt(2)
	ds_write_b32 v0, v56 offset:13520
	ds_write_b32 v146, v57 offset:13520
	ds_write_b32 v3, v58 offset:13520
	ds_write_b32 v2, v59 offset:13520
	s_waitcnt vmcnt(1)
	ds_write_b32 v0, v60 offset:14560
	ds_write_b32 v146, v61 offset:14560
	ds_write_b32 v3, v62 offset:14560
	ds_write_b32 v2, v63 offset:14560
	s_waitcnt vmcnt(0)
	ds_write_b32 v0, v64 offset:15600
	ds_write_b32 v146, v65 offset:15600
	ds_write_b32 v3, v66 offset:15600
	ds_write_b32 v2, v67 offset:15600
	s_waitcnt lgkmcnt(0)
	ds_read2_b32 v[2:3], v142 offset1:16
	ds_read2_b32 v[148:149], v142 offset0:65 offset1:81
	ds_read2_b32 v[154:155], v142 offset0:130 offset1:146
	ds_read2_b32 v[156:157], v142 offset0:195 offset1:211
	v_mov_b32_e32 v150, 0
	s_waitcnt lgkmcnt(3)
	v_mul_f32_e32 v0, 0x42000000, v2
	s_waitcnt lgkmcnt(2)
	v_mul_f32_e32 v2, 0x42000000, v148
	v_med3_f32 v0, v0, s41, v143
	s_waitcnt lgkmcnt(0)
	v_mul_f32_e32 v147, 0x42000000, v156
	v_med3_f32 v2, v2, s41, v143
	v_cvt_pk_fp8_f32 v150, v0, v2
	v_med3_f32 v2, v147, s41, v143
	v_add_u32_e32 v147, 0x400, v142
	ds_read2_b32 v[160:161], v147 offset0:4 offset1:20
	ds_read2_b32 v[162:163], v147 offset0:69 offset1:85
	ds_read2_b32 v[164:165], v147 offset0:134 offset1:150
	ds_read2_b32 v[166:167], v147 offset0:199 offset1:215
	v_mul_f32_e32 v146, 0x42000000, v154
	v_med3_f32 v0, v146, s41, v143
	v_cvt_pk_fp8_f32 v150, v0, v2 op_sel:[0,0,1]
	s_waitcnt lgkmcnt(3)
	v_mul_f32_e32 v0, 0x42000000, v160
	s_waitcnt lgkmcnt(2)
	v_mul_f32_e32 v2, 0x42000000, v162
	s_waitcnt lgkmcnt(0)
	v_mul_f32_e32 v148, 0x42000000, v166
	v_med3_f32 v0, v0, s41, v143
	v_med3_f32 v2, v2, s41, v143
	v_mov_b32_e32 v151, 0
	v_cvt_pk_fp8_f32 v151, v0, v2
	v_med3_f32 v2, v148, s41, v143
	v_add_u32_e32 v148, 0x800, v142
	ds_read2_b32 v[168:169], v148 offset0:8 offset1:24
	ds_read2_b32 v[170:171], v148 offset0:73 offset1:89
	ds_read2_b32 v[172:173], v148 offset0:138 offset1:154
	ds_read2_b32 v[174:175], v148 offset0:203 offset1:219
	v_mul_f32_e32 v146, 0x42000000, v164
	v_med3_f32 v0, v146, s41, v143
	v_cvt_pk_fp8_f32 v151, v0, v2 op_sel:[0,0,1]
	s_waitcnt lgkmcnt(3)
	v_mul_f32_e32 v0, 0x42000000, v168
	s_waitcnt lgkmcnt(2)
	v_mul_f32_e32 v2, 0x42000000, v170
	s_waitcnt lgkmcnt(1)
	v_mul_f32_e32 v146, 0x42000000, v172
	v_med3_f32 v0, v0, s41, v143
	v_med3_f32 v2, v2, s41, v143
	v_mov_b32_e32 v152, 0
	v_cvt_pk_fp8_f32 v152, v0, v2
	v_med3_f32 v0, v146, s41, v143
	v_add_u32_e32 v146, 0xc00, v142
	ds_read2_b32 v[176:177], v146 offset0:12 offset1:28
	ds_read2_b32 v[178:179], v146 offset0:77 offset1:93
	ds_read2_b32 v[180:181], v146 offset0:142 offset1:158
	s_waitcnt lgkmcnt(3)
	v_mul_f32_e32 v153, 0x42000000, v174
	v_med3_f32 v2, v153, s41, v143
	ds_read2_b32 v[182:183], v146 offset0:207 offset1:223
	v_cvt_pk_fp8_f32 v152, v0, v2 op_sel:[0,0,1]
	s_waitcnt lgkmcnt(3)
	v_mul_f32_e32 v0, 0x42000000, v176
	s_waitcnt lgkmcnt(2)
	v_mul_f32_e32 v2, 0x42000000, v178
	v_med3_f32 v0, v0, s41, v143
	v_med3_f32 v2, v2, s41, v143
	v_mov_b32_e32 v153, 0
	v_cvt_pk_fp8_f32 v153, v0, v2
	s_waitcnt lgkmcnt(1)
	v_mul_f32_e32 v154, 0x42000000, v180
	s_waitcnt lgkmcnt(0)
; #define LAS __attribute__((address_space(3)))
; #define GAS __attribute__((address_space(1)))
; __device__ __forceinline__ unsigned pk_fp8x4(float a, float b, float c, float d) { int p = __builtin_amdgcn_cvt_pk_fp8_f32(sat8(a), sat8(b), 0, false); p = __builtin_amdgcn_cvt_pk_fp8_f32(sat8(c), sat8(d), p, true); return (unsigned)p; }
; __device__ __forceinline__ void tr_finish(const TrDesc& d, f32x4 (&v)[16], LAS float* scr, int lane) {
;     ...
;         const int c = lane & 3, nl = lane >> 2; const LAS float* sp = scr + (16 * c) * 65 + nl; unsigned char* dp = d.dst + (size_t)nl * d.K + 16 * c;
; #pragma unroll
;         for (int j = 0; j < 4; ++j) { u32x4 o;
;             o.x = pk_fp8x4(sp[0 * 65 + 16 * j] * 32.0f, sp[1 * 65 + 16 * j] * 32.0f, sp[2 * 65 + 16 * j] * 32.0f, sp[3 * 65 + 16 * j] * 32.0f);
;             o.y = pk_fp8x4(sp[4 * 65 + 16 * j] * 32.0f, sp[5 * 65 + 16 * j] * 32.0f, sp[6 * 65 + 16 * j] * 32.0f, sp[7 * 65 + 16 * j] * 32.0f);
;             o.z = pk_fp8x4(sp[8 * 65 + 16 * j] * 32.0f, sp[9 * 65 + 16 * j] * 32.0f, sp[10 * 65 + 16 * j] * 32.0f, sp[11 * 65 + 16 * j] * 32.0f);
;             o.w = pk_fp8x4(sp[12 * 65 + 16 * j] * 32.0f, sp[13 * 65 + 16 * j] * 32.0f, sp[14 * 65 + 16 * j] * 32.0f, sp[15 * 65 + 16 * j] * 32.0f);
;             *(GAS u32x4*)(dp + (size_t)(16 * j) * d.K) = o; }
	v_mul_f32_e32 v0, 0x42000000, v182
	v_med3_f32 v2, v154, s41, v143
	v_med3_f32 v0, v0, s41, v143
	v_cvt_pk_fp8_f32 v153, v2, v0 op_sel:[0,0,1]
	v_mov_b64_e32 v[158:159], s[16:17]
	v_mad_i64_i32 v[158:159], s[22:23], s2, v132, v[158:159]
	v_lshl_add_u64 v[158:159], v[158:159], 0, v[134:135]
	v_mul_f32_e32 v0, 0x42000000, v3
	v_mul_f32_e32 v2, 0x42000000, v149
	global_store_dwordx4 v[158:159], v[150:153], off nt
	v_med3_f32 v0, v0, s41, v143
	v_med3_f32 v2, v2, s41, v143
	v_mov_b32_e32 v150, 0
	v_cvt_pk_fp8_f32 v150, v0, v2
	v_mul_f32_e32 v3, 0x42000000, v155
	v_mul_f32_e32 v0, 0x42000000, v157
	v_med3_f32 v2, v3, s41, v143
	v_med3_f32 v0, v0, s41, v143
	v_cvt_pk_fp8_f32 v150, v2, v0 op_sel:[0,0,1]
	v_mul_f32_e32 v0, 0x42000000, v161
	v_mul_f32_e32 v2, 0x42000000, v163
	v_med3_f32 v0, v0, s41, v143
	v_med3_f32 v2, v2, s41, v143
	v_mov_b32_e32 v151, 0
	v_cvt_pk_fp8_f32 v151, v0, v2
	v_mul_f32_e32 v3, 0x42000000, v165
	v_mul_f32_e32 v0, 0x42000000, v167
	v_med3_f32 v2, v3, s41, v143
	v_med3_f32 v0, v0, s41, v143
	v_cvt_pk_fp8_f32 v151, v2, v0 op_sel:[0,0,1]
	v_mul_f32_e32 v0, 0x42000000, v169
	v_mul_f32_e32 v2, 0x42000000, v171
	v_med3_f32 v0, v0, s41, v143
	v_med3_f32 v2, v2, s41, v143
	v_mov_b32_e32 v152, 0
	v_cvt_pk_fp8_f32 v152, v0, v2
	v_mul_f32_e32 v3, 0x42000000, v173
	v_mul_f32_e32 v0, 0x42000000, v175
	v_med3_f32 v2, v3, s41, v143
	v_med3_f32 v0, v0, s41, v143
	v_cvt_pk_fp8_f32 v152, v2, v0 op_sel:[0,0,1]
	v_mul_f32_e32 v0, 0x42000000, v177
	v_mul_f32_e32 v2, 0x42000000, v179
	v_med3_f32 v0, v0, s41, v143
	v_med3_f32 v2, v2, s41, v143
	v_mov_b32_e32 v153, 0
	v_cvt_pk_fp8_f32 v153, v0, v2
	s_ashr_i32 s3, s2, 31
	v_mul_f32_e32 v3, 0x42000000, v181
	v_mul_f32_e32 v0, 0x42000000, v183
	v_med3_f32 v2, v3, s41, v143
	v_med3_f32 v0, v0, s41, v143
	s_lshl_b64 s[22:23], s[2:3], 4
	v_cvt_pk_fp8_f32 v153, v2, v0 op_sel:[0,0,1]
	v_lshl_add_u64 v[2:3], v[158:159], 0, s[22:23]
	ds_read2_b32 v[154:155], v142 offset0:32 offset1:48
	ds_read2_b32 v[156:157], v142 offset0:97 offset1:113
	ds_read2_b32 v[158:159], v142 offset0:162 offset1:178
	ds_read2_b32 v[160:161], v142 offset0:227 offset1:243
	s_andn2_b64 vcc, exec, s[20:21]
	s_waitcnt lgkmcnt(3)
	v_mul_f32_e32 v0, 0x42000000, v154
	s_waitcnt lgkmcnt(2)
	v_mul_f32_e32 v149, 0x42000000, v156
	global_store_dwordx4 v[2:3], v[150:153], off nt
	v_med3_f32 v0, v0, s41, v143
	v_med3_f32 v149, v149, s41, v143
	v_mov_b32_e32 v150, 0
	v_cvt_pk_fp8_f32 v150, v0, v149
	ds_read2_b32 v[162:163], v147 offset0:36 offset1:52
	ds_read2_b32 v[164:165], v147 offset0:101 offset1:117
	ds_read2_b32 v[166:167], v147 offset0:166 offset1:182
	ds_read2_b32 v[168:169], v147 offset0:231 offset1:247
	s_waitcnt lgkmcnt(5)
	v_mul_f32_e32 v151, 0x42000000, v158
	s_waitcnt lgkmcnt(4)
	v_mul_f32_e32 v152, 0x42000000, v160
	v_med3_f32 v0, v151, s41, v143
	v_med3_f32 v149, v152, s41, v143
	v_cvt_pk_fp8_f32 v150, v0, v149 op_sel:[0,0,1]
	s_waitcnt lgkmcnt(3)
	v_mul_f32_e32 v0, 0x42000000, v162
	s_waitcnt lgkmcnt(2)
	v_mul_f32_e32 v149, 0x42000000, v164
	v_med3_f32 v0, v0, s41, v143
	v_med3_f32 v149, v149, s41, v143
	v_mov_b32_e32 v151, 0
	v_cvt_pk_fp8_f32 v151, v0, v149
	ds_read2_b32 v[170:171], v148 offset0:40 offset1:56
	ds_read2_b32 v[172:173], v148 offset0:105 offset1:121
	ds_read2_b32 v[174:175], v148 offset0:170 offset1:186
	ds_read2_b32 v[176:177], v148 offset0:235 offset1:251
	s_waitcnt lgkmcnt(5)
	v_mul_f32_e32 v152, 0x42000000, v166
	s_waitcnt lgkmcnt(4)
	v_mul_f32_e32 v153, 0x42000000, v168
	v_med3_f32 v0, v152, s41, v143
	v_med3_f32 v149, v153, s41, v143
	v_cvt_pk_fp8_f32 v151, v0, v149 op_sel:[0,0,1]
	s_waitcnt lgkmcnt(3)
	v_mul_f32_e32 v0, 0x42000000, v170
	s_waitcnt lgkmcnt(2)
	v_mul_f32_e32 v149, 0x42000000, v172
	v_med3_f32 v0, v0, s41, v143
	v_med3_f32 v149, v149, s41, v143
	v_mov_b32_e32 v152, 0
	v_cvt_pk_fp8_f32 v152, v0, v149
	ds_read2_b32 v[178:179], v146 offset0:44 offset1:60
	ds_read2_b32 v[180:181], v146 offset0:109 offset1:125
	ds_read2_b32 v[182:183], v146 offset0:174 offset1:190
	s_waitcnt lgkmcnt(4)
	v_mul_f32_e32 v153, 0x42000000, v174
	s_waitcnt lgkmcnt(3)
	v_mul_f32_e32 v154, 0x42000000, v176
	v_med3_f32 v0, v153, s41, v143
	v_med3_f32 v149, v154, s41, v143
	ds_read2_b32 v[184:185], v146 offset0:239 offset1:255
	v_cvt_pk_fp8_f32 v152, v0, v149 op_sel:[0,0,1]
	s_waitcnt lgkmcnt(3)
	v_mul_f32_e32 v0, 0x42000000, v178
	s_waitcnt lgkmcnt(2)
	v_mul_f32_e32 v149, 0x42000000, v180
	v_med3_f32 v0, v0, s41, v143
	v_med3_f32 v149, v149, s41, v143
	v_mov_b32_e32 v153, 0
	v_cvt_pk_fp8_f32 v153, v0, v149
	s_waitcnt lgkmcnt(1)
	v_mul_f32_e32 v154, 0x42000000, v182
	s_waitcnt lgkmcnt(0)
	v_mul_f32_e32 v0, 0x42000000, v184
	v_med3_f32 v149, v154, s41, v143
	v_med3_f32 v0, v0, s41, v143
	v_cvt_pk_fp8_f32 v153, v149, v0 op_sel:[0,0,1]
	v_mul_f32_e32 v0, 0x42000000, v155
	v_mul_f32_e32 v149, 0x42000000, v157
	v_med3_f32 v0, v0, s41, v143
	v_med3_f32 v149, v149, s41, v143
	v_mov_b32_e32 v154, 0
	v_cvt_pk_fp8_f32 v154, v0, v149
	v_mul_f32_e32 v155, 0x42000000, v159
	v_mul_f32_e32 v0, 0x42000000, v161
	v_med3_f32 v149, v155, s41, v143
	v_med3_f32 v0, v0, s41, v143
	v_cvt_pk_fp8_f32 v154, v149, v0 op_sel:[0,0,1]
	v_mul_f32_e32 v0, 0x42000000, v163
	v_mul_f32_e32 v149, 0x42000000, v165
	v_med3_f32 v0, v0, s41, v143
	v_med3_f32 v149, v149, s41, v143
	v_mov_b32_e32 v155, 0
	v_cvt_pk_fp8_f32 v155, v0, v149
	v_mul_f32_e32 v156, 0x42000000, v167
	v_mul_f32_e32 v0, 0x42000000, v169
	v_med3_f32 v149, v156, s41, v143
	v_med3_f32 v0, v0, s41, v143
	v_cvt_pk_fp8_f32 v155, v149, v0 op_sel:[0,0,1]
	v_mul_f32_e32 v0, 0x42000000, v171
	v_mul_f32_e32 v149, 0x42000000, v173
	v_med3_f32 v0, v0, s41, v143
	v_med3_f32 v149, v149, s41, v143
	v_mov_b32_e32 v156, 0
	v_cvt_pk_fp8_f32 v156, v0, v149
	v_mul_f32_e32 v157, 0x42000000, v175
	v_mul_f32_e32 v0, 0x42000000, v177
	v_med3_f32 v149, v157, s41, v143
	v_med3_f32 v0, v0, s41, v143
	v_cvt_pk_fp8_f32 v156, v149, v0 op_sel:[0,0,1]
	v_mul_f32_e32 v0, 0x42000000, v179
	v_mul_f32_e32 v149, 0x42000000, v181
	v_med3_f32 v0, v0, s41, v143
	v_med3_f32 v149, v149, s41, v143
	v_mov_b32_e32 v157, 0
	v_cvt_pk_fp8_f32 v157, v0, v149
	v_mul_f32_e32 v158, 0x42000000, v183
	v_mul_f32_e32 v0, 0x42000000, v185
	v_med3_f32 v149, v158, s41, v143
	v_med3_f32 v0, v0, s41, v143
	v_cvt_pk_fp8_f32 v157, v149, v0 op_sel:[0,0,1]
	v_lshl_add_u64 v[2:3], v[2:3], 0, s[22:23]
	global_store_dwordx4 v[2:3], v[150:153], off nt
	v_lshl_add_u64 v[2:3], v[2:3], 0, s[22:23]
	global_store_dwordx4 v[2:3], v[154:157], off nt
	s_waitcnt lgkmcnt(0)
	s_cbranch_vccnz .LBB0_71_hq
;     ...
;         auto decode = [&](int it) -> TrDesc {
;             TrDesc d; d.zero = 0; d.rope = 0; d.f8 = 0;
;             const int l = it / C_L; int r = it % C_L;
;             const float* W; unsigned char* WT; int ldw, K, k0, n0, scol, esz = 2;
;             if (r < C_IN) { const int kb = r / 188, nb = r % 188; n0 = 64 * nb; k0 = 64 * kb; ldw = NIN; K = D; W = a.w_in + (size_t)l * D * NIN;
;                 if (n0 < 3072) { d.rope = 1; scol = (n0 >> 7) * 128 + 32 * ((n0 >> 6) & 1) + 64 * (q4 >> 3) + 4 * (q4 & 7); }
;                 else if (n0 < 7680) scol = n0 + 4 * q4;
;                 else if (n0 < 11776) scol = n0 + 16 + 4 * q4;
;                 else if (n0 == 11776) { scol = (q4 < 4) ? 7680 + 4 * q4 : 0; d.zero = (q4 < 4) ? 0 : 1; }
;                 else { scol = 0; d.zero = 1; }
;     ...
;                 d.f8 = 1; esz = 1; WT = ws + WS_WIN + (size_t)l * NP * D;
;     ...
;                 WT = ws + WS_WIN + (size_t)l * NP * D * 2;
;     ...
;             } else if ((r -= C_IN) < C_OA) { const int kb = r / 32, nb = r % 32; n0 = 64 * nb; k0 = 64 * kb; ldw = D; K = 512; scol = n0 + 4 * q4; W = a.w_out_a + (size_t)l * 512 * D; WT = ws + WS_WOA + (size_t)l * D * 512 * (MIX_F8 ? 1 : 2); if (MIX_F8) { d.f8 = 1; esz = 1; }
;                 if (BR_FUSE) { K = 1536; WT = ws + WS_WOA + (size_t)l * D * 1536 + 1024; }
;             } else if ((r -= C_OA) < C_OB) { const int kb = r / 32, nb = r % 32; n0 = 64 * nb; k0 = 64 * kb; ldw = D; K = 1024; scol = n0 + 4 * q4; W = a.w_out_b + (size_t)l * 1024 * D; WT = ws + WS_WOB + (size_t)l * D * 1024 * (MIX_F8 ? 1 : 2); if (MIX_F8) { d.f8 = 1; esz = 1; }
;                 if (BR_FUSE) { K = 1536; WT = ws + WS_WOA + (size_t)l * D * 1536; }
;             } else if ((r -= C_OB) < C_O) { const int kb = r / 32, nb = r % 32; n0 = 64 * nb; k0 = 64 * kb; ldw = D; K = D; scol = n0 + 4 * q4; W = a.w_out + (size_t)l * D * D; WT = ws + WS_WO + (size_t)l * D * D * (MIX_F8 ? 1 : 2); if (MIX_F8) { d.f8 = 1; esz = 1; }
;             } else if ((r -= C_O) < C_GU) { const int e = r / 1024, r2 = r % 1024, kb = r2 / 32, nb = r2 % 32, pn = nb >> 2, sgu = (nb >> 1) & 1, c0 = 64 * (nb & 1);
;     ...
;             if (itB >= NIT) break;
;             const int itA = itB + NGW;
;             if (itA < NIT) { dA = decode(NIT - 1 - itA); tr_load(dA, vA); }
;             tr_finish(dB, vB, scr, lane);
;             it = itA;
;         }
	s_lshr_b32 s42, s44, 6
	s_lshl_b32 s42, s42, 3
	s_bfe_u32 s100, s44, 0x30002
	s_or_b32 s42, s42, s100
	s_add_i32 s42, s42, 24
	s_and_b32 s100, s42, 7
	s_lshr_b32 s42, s42, 3
	s_lshl_b32 s42, s42, 6
	s_lshl_b32 s100, s100, 2
	s_or_b32 s42, s42, s100
	s_and_b32 s100, s44, 0x23
	s_or_b32 s42, s42, s100
	s_cmp_ge_i32 s42, s101
	s_cbranch_scc1 .LBB0_144_hq
	s_sub_i32 s2, 0xfcff, s42
	s_mul_hi_u32 s0, s2, 0x81848da9
	s_lshr_b32 s0, s0, 14
	s_mul_i32 s3, s0, 0x7e80
	s_sub_i32 s27, s2, s3
	s_cmpk_gt_u32 s27, 0x177f
	s_cbranch_scc0 .LBB0_117_hq
	s_cmpk_gt_u32 s27, 0x187f
	s_cbranch_scc0 .LBB0_119_hq
	s_cmpk_gt_u32 s27, 0x1a7f
	s_cbranch_scc0 .LBB0_120_hq
	s_cmpk_gt_u32 s27, 0x1e7f
	s_cbranch_scc0 .LBB0_123_hq
	s_lshl_b32 s22, s27, 6
	s_cmpk_gt_u32 s27, 0x5e7f
	s_cbranch_scc0 .LBB0_147_hq
	s_add_i32 s2, s27, 0xffffa180
	s_lshr_b32 s16, s2, 9
	s_lshl_b32 s2, s2, 1
	s_and_b32 s44, s2, 0x3c0
	s_load_dwordx2 s[2:3], s[8:9], 0x88
	s_lshl_b32 s17, s0, 4
	s_add_i32 s20, s16, s17
	s_mov_b32 s21, s1
	s_and_b32 s15, s22, 0x7c0
	s_lshl_b64 s[16:17], s[20:21], 23
	s_waitcnt lgkmcnt(0)
	s_add_u32 s16, s2, s16
	s_addc_u32 s17, s3, s17
	s_lshl_b64 s[2:3], s[20:21], 21
	s_add_u32 s20, s28, s2
	v_or_b32_e32 v0, s15, v136
	s_addc_u32 s21, s29, s3
	s_cbranch_execz .LBB0_148_hq
	s_movk_i32 s2, 0x400
	s_mov_b64 s[22:23], 0x800
	s_cbranch_execz .LBB0_124_hq
	s_branch .LBB0_125_hq
